# F1 with 48 bytes of padding before both key loops (code placement: loop bodies start at a different 64-byte phase)
# baseline (speedup 1.0000x reference)
.LBB0_756:
	s_and_b32 s8, s8, 7
	s_ashr_i32 s31, s30, 31
	s_mul_i32 s7, s30, 0xc00
	s_mul_hi_i32 s6, s30, 0xc00
	s_add_u32 s7, s37, s7
	s_addc_u32 s6, s38, s6
	s_mul_i32 s9, s8, 0x180
	s_add_u32 s10, s7, s9
	s_addc_u32 s11, s6, 0
	s_add_u32 s6, s39, s9
	s_addc_u32 s7, s40, 0
	s_lshl_b32 s61, s8, 7
	s_lshl_b32 s8, s8, 8
	s_add_u32 s34, s41, s8
	v_readfirstlane_b32 s9, v254
	s_addc_u32 s35, s42, 0
	s_ashr_i32 s8, s9, 6
	s_lshl_b32 s82, s8, 10
	s_mov_b32 s72, s6
	s_and_b32 s73, s7, 0xffff
	s_mov_b32 s74, 0x7ffffff0
	s_mov_b32 s75, 0x20000
	s_mov_b32 s76, s34
	s_and_b32 s77, s35, 0xffff
	s_mov_b32 s78, 0x7ffffff0
	s_mov_b32 s79, 0x20000
	v_lshl_or_b32 v2, s8, 5, v188
	v_mov_b64_e32 v[0:1], s[10:11]
	v_mad_i64_i32 v[0:1], s[10:11], v2, s46, v[0:1]
	v_lshl_add_u64 v[26:27], s[26:27], 0, v[142:143]
	v_lshl_add_u64 v[28:29], v[146:147], 0, s[26:27]
	v_lshl_add_u64 v[38:39], v[0:1], 0, v[148:149]
	v_lshlrev_b64 v[0:1], 11, v[26:27]
	v_lshlrev_b64 v[18:19], 11, v[28:29]
	v_lshl_add_u64 v[0:1], s[34:35], 0, v[0:1]
	v_lshl_add_u64 v[18:19], s[34:35], 0, v[18:19]
	v_lshl_add_u64 v[0:1], v[0:1], 0, v[150:151]
	v_lshl_add_u64 v[22:23], v[18:19], 0, v[150:151]
	global_load_dwordx4 v[2:5], v[38:39], off offset:256
	global_load_dwordx4 v[6:9], v[38:39], off offset:288
	global_load_dwordx4 v[10:13], v[38:39], off offset:320
	global_load_dwordx4 v[14:17], v[38:39], off offset:352
	global_load_dwordx4 v[18:21], v[0:1], off
	s_nop 0
	global_load_dwordx4 v[22:25], v[22:23], off
	v_mov_b64_e32 v[0:1], s[6:7]
	v_mad_u64_u32 v[30:31], s[10:11], v26, s46, v[0:1]
	v_mad_i32_i24 v31, v27, s46, v31
	v_lshl_add_u64 v[26:27], v[30:31], 0, v[150:151]
	v_mad_u64_u32 v[30:31], s[10:11], v28, s46, v[0:1]
	v_mad_i32_i24 v31, v29, s46, v31
	v_lshl_add_u64 v[30:31], v[30:31], 0, v[150:151]
	v_lshl_add_u64 v[34:35], s[26:27], 0, v[144:145]
	global_load_dwordx4 v[26:29], v[26:27], off
	s_nop 0
	global_load_dwordx4 v[30:33], v[30:31], off
	v_mad_u64_u32 v[36:37], s[10:11], v34, s46, v[0:1]
	v_mad_i32_i24 v37, v35, s46, v37
	v_lshl_add_u64 v[34:35], v[36:37], 0, v[152:153]
	global_load_dwordx4 v[34:37], v[34:35], off offset:256
	s_nop 0
	global_load_dwordx4 v[124:127], v[38:39], off
	global_load_dwordx4 v[120:123], v[38:39], off offset:32
	global_load_dwordx4 v[116:119], v[38:39], off offset:64
	global_load_dwordx4 v[112:115], v[38:39], off offset:96
	global_load_dwordx4 v[108:111], v[38:39], off offset:128
	global_load_dwordx4 v[104:107], v[38:39], off offset:160
	global_load_dwordx4 v[100:103], v[38:39], off offset:192
	global_load_dwordx4 v[96:99], v[38:39], off offset:224
	s_lshl_b32 s8, s8, 12
	v_add_u32_e32 v190, s8, v166
	v_add_u32_e32 v191, s47, v170
	v_add_u32_e32 v192, s47, v171
	v_add_u32_e32 v193, s47, v172
	v_add_u32_e32 v194, s47, v173
	s_and_b32 s9, s9, 0x3fffffc0
	s_lshl_b32 s9, s9, 2
	s_add_i32 s62, s9, 0
	s_add_i32 s62, s62, 0x14000
	s_mov_b32 s11, s27
	s_mov_b32 s22, s27
	s_mov_b32 s23, s27
	s_mov_b32 s8, s27
	s_mov_b32 s9, s27
	s_mov_b32 s12, s27
	s_mov_b32 s13, s27
	s_mov_b32 s14, s27
	s_mov_b32 s15, s27
	s_mov_b32 s16, s27
	s_mov_b32 s17, s27
	s_mov_b32 s18, s27
	s_mov_b32 s19, s27
	s_mov_b32 s20, s27
	s_mov_b32 s21, s27
	v_add_u32_e32 v195, 0, v168
	s_mov_b32 s64, 2
	v_mov_b32_e32 v140, 0
	v_add_u32_e32 v196, 0x12000, v195
	v_lshrrev_b32_e32 v156, 4, v254
	v_and_b32_e32 v157, 15, v156
	v_and_b32_e32 v159, 15, v254
	v_xor_b32_e32 v157, v157, v159
	v_lshlrev_b32_e32 v157, 4, v157
	v_mad_u32_u24 v154, v156, s46, v157
	v_lshrrev_b32_e32 v156, 3, v254
	v_bfe_u32 v157, v254, 4, 3
	v_and_b32_e32 v159, 7, v254
	v_xor_b32_e32 v157, v157, v159
	v_lshlrev_b32_e32 v157, 4, v157
	v_add_u32_e32 v157, 0x100, v157
	v_mad_u32_u24 v155, v156, s46, v157
	v_and_b32_e32 v158, 3, v254
	v_lshlrev_b32_e32 v158, 4, v158
	v_bfe_u32 v156, v254, 5, 2
	v_lshl_or_b32 v158, v156, 6, v158
	v_bfe_u32 v156, v254, 2, 2
	v_lshl_or_b32 v158, v156, 11, v158
	v_bfe_u32 v156, v254, 7, 1
	v_lshl_or_b32 v158, v156, 13, v158
	v_bfe_u32 v156, v254, 4, 1
	v_lshl_or_b32 v158, v156, 14, v158
	v_bfe_u32 v156, v254, 8, 1
	v_lshl_or_b32 v158, v156, 15, v158
	v_lshl_add_u32 v189, v188, 2, s62
	s_waitcnt vmcnt(16)
	ds_write_b128 v190, v[2:5]
	s_waitcnt vmcnt(15)
	ds_write_b128 v190, v[6:9] offset:1024
	s_waitcnt vmcnt(14)
	ds_write_b128 v190, v[10:13] offset:2048
	s_waitcnt vmcnt(13)
	ds_write_b128 v190, v[14:17] offset:3072
	s_waitcnt vmcnt(0)
	s_waitcnt vmcnt(12)
	ds_write_b128 v175, v[18:21]
	s_waitcnt vmcnt(11)
	ds_write_b128 v176, v[22:25]
	s_waitcnt vmcnt(10)
	ds_write_b128 v177, v[26:29] offset:32768
	s_waitcnt vmcnt(9)
	ds_write_b128 v178, v[30:33] offset:32768
	s_waitcnt vmcnt(8)
	ds_write_b128 v179, v[34:37]
	s_waitcnt lgkmcnt(0)
	s_barrier
	ds_read_b128 v[2:5], v180 offset:32768
	ds_read_b128 v[6:9], v180 offset:40960
	s_waitcnt vmcnt(7) lgkmcnt(1)
	v_mfma_f32_32x32x16_bf16 v[48:63], v[2:5], v[124:127], 0
	s_waitcnt lgkmcnt(0)
	v_mfma_f32_32x32x16_bf16 v[64:79], v[6:9], v[124:127], 0
	ds_read_b128 v[2:5], v181 offset:32768
	ds_read_b128 v[6:9], v181 offset:40960
	s_waitcnt vmcnt(6) lgkmcnt(1)
	v_mfma_f32_32x32x16_bf16 v[48:63], v[2:5], v[120:123], v[48:63]
	s_waitcnt lgkmcnt(0)
	v_mfma_f32_32x32x16_bf16 v[64:79], v[6:9], v[120:123], v[64:79]
	ds_read_b128 v[2:5], v182 offset:32768
	ds_read_b128 v[6:9], v182 offset:40960
	s_waitcnt vmcnt(5) lgkmcnt(1)
	v_mfma_f32_32x32x16_bf16 v[48:63], v[2:5], v[116:119], v[48:63]
	s_waitcnt lgkmcnt(0)
	v_mfma_f32_32x32x16_bf16 v[64:79], v[6:9], v[116:119], v[64:79]
	ds_read_b128 v[2:5], v183 offset:32768
	ds_read_b128 v[6:9], v183 offset:40960
	s_waitcnt vmcnt(4) lgkmcnt(1)
	v_mfma_f32_32x32x16_bf16 v[48:63], v[2:5], v[112:115], v[48:63]
	s_waitcnt lgkmcnt(0)
	v_mfma_f32_32x32x16_bf16 v[64:79], v[6:9], v[112:115], v[64:79]
	ds_read_b128 v[2:5], v184 offset:32768
	ds_read_b128 v[6:9], v184 offset:40960
	s_waitcnt vmcnt(3) lgkmcnt(1)
	v_mfma_f32_32x32x16_bf16 v[48:63], v[2:5], v[108:111], v[48:63]
	s_waitcnt lgkmcnt(0)
	v_mfma_f32_32x32x16_bf16 v[64:79], v[6:9], v[108:111], v[64:79]
	ds_read_b128 v[2:5], v185 offset:32768
	ds_read_b128 v[6:9], v185 offset:40960
	s_waitcnt vmcnt(2) lgkmcnt(1)
	v_mfma_f32_32x32x16_bf16 v[48:63], v[2:5], v[104:107], v[48:63]
	s_waitcnt lgkmcnt(0)
	v_mfma_f32_32x32x16_bf16 v[64:79], v[6:9], v[104:107], v[64:79]
	ds_read_b128 v[2:5], v186 offset:32768
	ds_read_b128 v[6:9], v186 offset:40960
	s_waitcnt vmcnt(1) lgkmcnt(1)
	v_mfma_f32_32x32x16_bf16 v[48:63], v[2:5], v[100:103], v[48:63]
	s_waitcnt lgkmcnt(0)
	v_mfma_f32_32x32x16_bf16 v[64:79], v[6:9], v[100:103], v[64:79]
	ds_read_b128 v[2:5], v187 offset:32768
	ds_read_b128 v[6:9], v187 offset:40960
	s_waitcnt vmcnt(0) lgkmcnt(1)
	v_mfma_f32_32x32x16_bf16 v[48:63], v[2:5], v[96:99], v[48:63]
	s_waitcnt lgkmcnt(0)
	v_mfma_f32_32x32x16_bf16 v[64:79], v[6:9], v[96:99], v[64:79]
	ds_read_b128 v[2:5], v191
	ds_read_b128 v[6:9], v190
	ds_read_b128 v[10:13], v191 offset:4096
	ds_read_b128 v[14:17], v190 offset:1024
	s_waitcnt lgkmcnt(2)
	v_mfma_f32_32x32x16_bf16 v[48:63], v[2:5], v[6:9], v[48:63]
	s_waitcnt lgkmcnt(1)
	v_mfma_f32_32x32x16_bf16 v[64:79], v[10:13], v[6:9], v[64:79]
	ds_read_b128 v[2:5], v192
	ds_read_b128 v[6:9], v192 offset:4096
	s_waitcnt lgkmcnt(1)
	v_mfma_f32_32x32x16_bf16 v[48:63], v[2:5], v[14:17], v[48:63]
	s_waitcnt lgkmcnt(0)
	v_mfma_f32_32x32x16_bf16 v[64:79], v[6:9], v[14:17], v[64:79]
	ds_read_b128 v[2:5], v193
	ds_read_b128 v[6:9], v190 offset:2048
	ds_read_b128 v[10:13], v193 offset:4096
	ds_read_b128 v[14:17], v190 offset:3072
	s_waitcnt lgkmcnt(2)
	v_mfma_f32_32x32x16_bf16 v[48:63], v[2:5], v[6:9], v[48:63]
	s_waitcnt lgkmcnt(1)
	v_mfma_f32_32x32x16_bf16 v[64:79], v[10:13], v[6:9], v[64:79]
	ds_read_b128 v[2:5], v194
	ds_read_b128 v[6:9], v194 offset:4096
	s_waitcnt lgkmcnt(1)
	v_mfma_f32_32x32x16_bf16 v[48:63], v[2:5], v[14:17], v[48:63]
	s_waitcnt lgkmcnt(0)
	v_mfma_f32_32x32x16_bf16 v[64:79], v[6:9], v[14:17], v[64:79]
	s_nop 9
	v_max_f32_e32 v2, v49, v49
	v_max_f32_e32 v3, v48, v48
	v_max_f32_e32 v2, v3, v2
	v_max3_f32 v2, v2, v50, v51
	v_max3_f32 v2, v2, v52, v53
	v_max3_f32 v2, v2, v54, v55
	v_max3_f32 v2, v2, v56, v57
	v_max3_f32 v2, v2, v58, v59
	v_max3_f32 v2, v2, v60, v61
	v_max3_f32 v2, v2, v62, v63
	v_max3_f32 v2, v2, v64, v65
	v_max3_f32 v2, v2, v66, v67
	v_max3_f32 v2, v2, v68, v69
	v_max3_f32 v2, v2, v70, v71
	v_max3_f32 v2, v2, v72, v73
	v_max3_f32 v2, v2, v74, v75
	v_max3_f32 v2, v2, v76, v77
	v_max3_f32 v2, v2, v78, v79
	v_mov_b32_e32 v3, v2
	s_nop 1
	v_permlane32_swap_b32_e32 v2, v3
	v_max_f32_e32 v3, v3, v3
	v_max_f32_e32 v2, v2, v2
	v_max_f32_e32 v2, v2, v3
	v_add_f32_e32 v3, 0x7149f2ca, v2
	v_cmp_ge_f32_e32 vcc, s48, v3
	s_cmp_eq_u64 vcc, exec
	s_cselect_b64 vcc, -1, 0
	s_add_i32 s10, s26, 64
	v_max_f32_e32 v128, 0xf149f2ca, v2
	v_lshl_add_u64 v[2:3], s[10:11], 0, v[142:143]
	v_lshl_add_u64 v[4:5], v[146:147], 0, s[10:11]
	v_lshl_add_u64 v[6:7], s[10:11], 0, v[144:145]
	v_lshlrev_b64 v[8:9], 11, v[2:3]
	v_lshlrev_b64 v[10:11], 11, v[4:5]
	v_mad_u64_u32 v[12:13], s[10:11], v2, s46, v[0:1]
	v_mad_u64_u32 v[14:15], s[10:11], v4, s46, v[0:1]
	v_mad_u64_u32 v[0:1], s[10:11], v6, s46, v[0:1]
	v_lshl_add_u64 v[8:9], s[34:35], 0, v[8:9]
	v_lshl_add_u64 v[10:11], s[34:35], 0, v[10:11]
	v_mad_i32_i24 v13, v3, s46, v13
	v_mad_i32_i24 v15, v5, s46, v15
	v_mad_i32_i24 v1, v7, s46, v1
	v_lshl_add_u64 v[2:3], v[8:9], 0, v[150:151]
	v_lshl_add_u64 v[4:5], v[10:11], 0, v[150:151]
	v_lshl_add_u64 v[6:7], v[12:13], 0, v[150:151]
	v_lshl_add_u64 v[8:9], v[14:15], 0, v[150:151]
	v_lshl_add_u64 v[0:1], v[0:1], 0, v[152:153]
	global_load_dwordx4 v[80:83], v[2:3], off
	global_load_dwordx4 v[84:87], v[4:5], off
	global_load_dwordx4 v[88:91], v[6:7], off
	global_load_dwordx4 v[92:95], v[8:9], off
	global_load_dwordx4 v[200:203], v[0:1], off offset:256
	v_sub_f32_e32 v129, 0xf149f2ca, v128
	v_mul_f32_e32 v129, 0x3dd53b94, v129
	v_exp_f32_e32 v164, v129
	v_mov_b32_e32 v129, 0xf149f2ca
	v_cndmask_b32_e32 v198, v128, v129, vcc
	v_mul_f32_e32 v138, 0xbdd53b94, v198
	v_mov_b32_e32 v165, v138
	v_fmamk_f32 v48, v48, 0x3dd53b94, v138
	v_fmamk_f32 v49, v49, 0x3dd53b94, v138
	v_fmamk_f32 v50, v50, 0x3dd53b94, v138
	v_fmamk_f32 v51, v51, 0x3dd53b94, v138
	v_fmamk_f32 v52, v52, 0x3dd53b94, v138
	v_fmamk_f32 v53, v53, 0x3dd53b94, v138
	v_fmamk_f32 v54, v54, 0x3dd53b94, v138
	v_fmamk_f32 v55, v55, 0x3dd53b94, v138
	v_fmamk_f32 v56, v56, 0x3dd53b94, v138
	v_fmamk_f32 v57, v57, 0x3dd53b94, v138
	v_fmamk_f32 v58, v58, 0x3dd53b94, v138
	v_fmamk_f32 v59, v59, 0x3dd53b94, v138
	v_fmamk_f32 v60, v60, 0x3dd53b94, v138
	v_fmamk_f32 v61, v61, 0x3dd53b94, v138
	v_fmamk_f32 v62, v62, 0x3dd53b94, v138
	v_fmac_f32_e32 v165, 0x3dd53b94, v63
	s_mov_b32 s10, s27
	s_mov_b32 s11, s27
	v_mov_b64_e32 v[30:31], s[22:23]
	v_exp_f32_e32 v222, v48
	v_exp_f32_e32 v224, v49
	v_exp_f32_e32 v220, v50
	v_exp_f32_e32 v223, v51
	v_exp_f32_e32 v219, v52
	v_exp_f32_e32 v221, v53
	v_exp_f32_e32 v217, v54
	v_exp_f32_e32 v218, v55
	v_exp_f32_e32 v212, v56
	v_exp_f32_e32 v214, v57
	v_exp_f32_e32 v211, v58
	v_exp_f32_e32 v213, v59
	v_exp_f32_e32 v208, v60
	v_exp_f32_e32 v210, v61
	v_exp_f32_e32 v207, v62
	v_exp_f32_e32 v209, v165
	v_mov_b64_e32 v[16:17], s[8:9]
	s_waitcnt vmcnt(0)
	v_mov_b64_e32 v[28:29], s[20:21]
	v_mov_b64_e32 v[26:27], s[18:19]
	v_mov_b64_e32 v[24:25], s[16:17]
	v_mov_b64_e32 v[22:23], s[14:15]
	v_mov_b64_e32 v[20:21], s[12:13]
	v_mov_b64_e32 v[18:19], s[10:11]
	v_mov_b64_e32 v[46:47], v[30:31]
	v_mov_b64_e32 v[0:1], v[16:17]
	v_mov_b64_e32 v[62:63], v[30:31]
	v_mov_b64_e32 v[44:45], v[28:29]
	v_mov_b64_e32 v[42:43], v[26:27]
	v_mov_b64_e32 v[40:41], v[24:25]
	v_mov_b64_e32 v[38:39], v[22:23]
	v_mov_b64_e32 v[36:37], v[20:21]
	v_mov_b64_e32 v[34:35], v[18:19]
	v_mov_b64_e32 v[32:33], v[16:17]
	v_mov_b64_e32 v[2:3], v[18:19]
	v_mov_b64_e32 v[4:5], v[20:21]
	v_mov_b64_e32 v[6:7], v[22:23]
	v_mov_b64_e32 v[8:9], v[24:25]
	v_mov_b64_e32 v[10:11], v[26:27]
	v_mov_b64_e32 v[12:13], v[28:29]
	v_mov_b64_e32 v[14:15], v[30:31]
	s_add_i32 s10, s26, 0x80
	s_add_i32 s83, s26, 64
	s_sub_i32 s11, s65, 64
	v_pk_fma_f32 v[134:135], v[78:79], s[28:29], v[138:139] op_sel_hi:[1,0,0]
	v_pk_fma_f32 v[160:161], v[76:77], s[28:29], v[138:139] op_sel_hi:[1,0,0]
	v_pk_fma_f32 v[162:163], v[74:75], s[28:29], v[138:139] op_sel_hi:[1,0,0]
	v_pk_fma_f32 v[128:129], v[72:73], s[28:29], v[138:139] op_sel_hi:[1,0,0]
	v_pk_fma_f32 v[130:131], v[70:71], s[28:29], v[138:139] op_sel_hi:[1,0,0]
	v_pk_fma_f32 v[132:133], v[68:69], s[28:29], v[138:139] op_sel_hi:[1,0,0]
	v_pk_fma_f32 v[136:137], v[66:67], s[28:29], v[138:139] op_sel_hi:[1,0,0]
	v_pk_fma_f32 v[138:139], v[64:65], s[28:29], v[138:139] op_sel_hi:[1,0,0]
	v_cndmask_b32_e64 v197, v164, 1.0, vcc
	v_mov_b64_e32 v[60:61], v[28:29]
	v_mov_b64_e32 v[58:59], v[26:27]
	v_mov_b64_e32 v[56:57], v[24:25]
	v_mov_b64_e32 v[54:55], v[22:23]
	v_mov_b64_e32 v[52:53], v[20:21]
	v_mov_b64_e32 v[50:51], v[18:19]
	v_mov_b64_e32 v[48:49], v[16:17]
	s_waitcnt vmcnt(4)
	ds_write_b128 v175, v[80:83] offset:16384
	s_waitcnt vmcnt(3)
	ds_write_b128 v176, v[84:87] offset:16384
	s_waitcnt vmcnt(2)
	ds_write_b128 v177, v[88:91] offset:49152
	s_waitcnt vmcnt(1)
	ds_write_b128 v178, v[92:95] offset:49152
	s_waitcnt vmcnt(0)
	ds_write_b128 v196, v[200:203]
	s_nop 0
	s_nop 0
	s_nop 0
	s_nop 0
	s_nop 0
	s_nop 0
	s_nop 0
	s_nop 0
	s_nop 0
	s_nop 0
	s_nop 0
	s_nop 0
	s_waitcnt lgkmcnt(0)
	s_barrier

.LBB0_2011:
	s_ashr_i32 s6, s11, 3
	s_lshl_b32 s60, s6, 8
	s_lshl_b32 s61, s6, 12
	s_lshl_b32 s6, s10, 8
	s_and_b32 s6, s6, 0xf00
	s_or_b32 s28, s61, s6
	s_add_i32 s8, s60, 0x4000
	s_and_b32 s12, s11, 7
	s_ashr_i32 s29, s28, 31
	s_mul_i32 s7, s28, 0xc00
	s_mul_hi_i32 s6, s28, 0xc00
	s_add_u32 s7, s35, s7
	s_addc_u32 s6, s36, s6
	s_mul_i32 s13, s12, 0x180
	s_add_u32 s10, s7, s13
	s_addc_u32 s11, s6, 0
	s_add_u32 s6, s37, s13
	s_addc_u32 s7, s38, 0
	s_lshl_b32 s59, s12, 7
	s_lshl_b32 s12, s12, 8
	s_add_u32 s30, s39, s12
	v_readfirstlane_b32 s62, v254
	s_addc_u32 s31, s40, 0
	s_ashr_i32 s12, s62, 6
	s_lshl_b32 s82, s12, 10
	s_mov_b32 s72, s6
	s_and_b32 s73, s7, 0xffff
	s_mov_b32 s74, 0x7ffffff0
	s_mov_b32 s75, 0x20000
	s_mov_b32 s76, s30
	s_and_b32 s77, s31, 0xffff
	s_mov_b32 s78, 0x7ffffff0
	s_mov_b32 s79, 0x20000
	v_lshl_add_u64 v[26:27], s[8:9], 0, v[142:143]
	v_lshl_add_u64 v[28:29], v[146:147], 0, s[8:9]
	v_lshl_or_b32 v2, s12, 5, v188
	v_mov_b64_e32 v[0:1], s[10:11]
	v_lshlrev_b64 v[16:17], 11, v[26:27]
	v_lshlrev_b64 v[18:19], 11, v[28:29]
	v_mad_i64_i32 v[0:1], s[10:11], v2, s44, v[0:1]
	v_lshl_add_u64 v[16:17], s[30:31], 0, v[16:17]
	v_lshl_add_u64 v[18:19], s[30:31], 0, v[18:19]
	v_lshl_add_u64 v[38:39], v[0:1], 0, v[148:149]
	v_lshl_add_u64 v[16:17], v[16:17], 0, v[150:151]
	v_lshl_add_u64 v[22:23], v[18:19], 0, v[150:151]
	global_load_dwordx4 v[0:3], v[38:39], off offset:256
	global_load_dwordx4 v[4:7], v[38:39], off offset:288
	global_load_dwordx4 v[8:11], v[38:39], off offset:320
	global_load_dwordx4 v[12:15], v[38:39], off offset:352
	global_load_dwordx4 v[18:21], v[16:17], off
	s_nop 0
	global_load_dwordx4 v[22:25], v[22:23], off
	v_mov_b64_e32 v[16:17], s[6:7]
	v_mad_u64_u32 v[30:31], s[10:11], v26, s44, v[16:17]
	v_mad_i32_i24 v31, v27, s44, v31
	v_lshl_add_u64 v[26:27], v[30:31], 0, v[150:151]
	v_mad_u64_u32 v[30:31], s[10:11], v28, s44, v[16:17]
	v_mad_i32_i24 v31, v29, s44, v31
	v_lshl_add_u64 v[30:31], v[30:31], 0, v[150:151]
	v_lshl_add_u64 v[34:35], s[8:9], 0, v[144:145]
	global_load_dwordx4 v[26:29], v[26:27], off
	s_nop 0
	global_load_dwordx4 v[30:33], v[30:31], off
	v_mad_u64_u32 v[36:37], s[10:11], v34, s44, v[16:17]
	v_mad_i32_i24 v37, v35, s44, v37
	v_lshl_add_u64 v[34:35], v[36:37], 0, v[152:153]
	global_load_dwordx4 v[34:37], v[34:35], off offset:256
	s_nop 0
	global_load_dwordx4 v[124:127], v[38:39], off
	global_load_dwordx4 v[120:123], v[38:39], off offset:32
	global_load_dwordx4 v[116:119], v[38:39], off offset:64
	global_load_dwordx4 v[112:115], v[38:39], off offset:96
	global_load_dwordx4 v[108:111], v[38:39], off offset:128
	global_load_dwordx4 v[104:107], v[38:39], off offset:160
	global_load_dwordx4 v[100:103], v[38:39], off offset:192
	global_load_dwordx4 v[96:99], v[38:39], off offset:224
	s_lshl_b32 s8, s12, 12
	v_add_u32_e32 v190, s8, v166
	v_add_u32_e32 v191, s45, v170
	v_add_u32_e32 v192, s45, v171
	v_add_u32_e32 v193, s45, v172
	v_add_u32_e32 v194, s45, v173
	s_mov_b32 s8, s9
	s_mov_b32 s10, s9
	s_mov_b32 s11, s9
	s_mov_b32 s12, s9
	s_mov_b32 s13, s9
	s_mov_b32 s14, s9
	s_mov_b32 s15, s9
	s_mov_b32 s16, s9
	s_mov_b32 s17, s9
	s_mov_b32 s18, s9
	s_mov_b32 s19, s9
	s_mov_b32 s20, s9
	s_mov_b32 s21, s9
	s_mov_b32 s22, s9
	s_mov_b32 s23, s9
	v_add_u32_e32 v195, 0, v168
	v_mov_b32_e32 v140, 0
	v_add_u32_e32 v196, 0x12000, v195
	v_lshrrev_b32_e32 v156, 4, v254
	v_and_b32_e32 v157, 15, v156
	v_and_b32_e32 v159, 15, v254
	v_xor_b32_e32 v157, v157, v159
	v_lshlrev_b32_e32 v157, 4, v157
	v_mad_u32_u24 v154, v156, s44, v157
	v_lshrrev_b32_e32 v156, 3, v254
	v_bfe_u32 v157, v254, 4, 3
	v_and_b32_e32 v159, 7, v254
	v_xor_b32_e32 v157, v157, v159
	v_lshlrev_b32_e32 v157, 4, v157
	v_add_u32_e32 v157, 0x100, v157
	v_mad_u32_u24 v155, v156, s44, v157
	v_and_b32_e32 v158, 3, v254
	v_lshlrev_b32_e32 v158, 4, v158
	v_bfe_u32 v156, v254, 5, 2
	v_lshl_or_b32 v158, v156, 6, v158
	v_bfe_u32 v156, v254, 2, 2
	v_lshl_or_b32 v158, v156, 11, v158
	v_bfe_u32 v156, v254, 7, 1
	v_lshl_or_b32 v158, v156, 13, v158
	v_bfe_u32 v156, v254, 4, 1
	v_lshl_or_b32 v158, v156, 14, v158
	v_bfe_u32 v156, v254, 8, 1
	v_lshl_or_b32 v158, v156, 15, v158
	s_waitcnt vmcnt(16)
	ds_write_b128 v190, v[0:3]
	s_waitcnt vmcnt(15)
	ds_write_b128 v190, v[4:7] offset:1024
	s_waitcnt vmcnt(14)
	ds_write_b128 v190, v[8:11] offset:2048
	s_waitcnt vmcnt(13)
	ds_write_b128 v190, v[12:15] offset:3072
	s_waitcnt vmcnt(0)
	s_waitcnt vmcnt(12)
	ds_write_b128 v175, v[18:21]
	s_waitcnt vmcnt(11)
	ds_write_b128 v176, v[22:25]
	s_waitcnt vmcnt(10)
	ds_write_b128 v177, v[26:29] offset:32768
	s_waitcnt vmcnt(9)
	ds_write_b128 v178, v[30:33] offset:32768
	s_waitcnt vmcnt(8)
	ds_write_b128 v179, v[34:37]
	s_waitcnt lgkmcnt(0)
	s_barrier
	ds_read_b128 v[0:3], v180 offset:32768
	ds_read_b128 v[4:7], v180 offset:40960
	s_waitcnt vmcnt(7) lgkmcnt(1)
	v_mfma_f32_32x32x16_bf16 v[48:63], v[0:3], v[124:127], 0
	s_waitcnt lgkmcnt(0)
	v_mfma_f32_32x32x16_bf16 v[64:79], v[4:7], v[124:127], 0
	ds_read_b128 v[0:3], v181 offset:32768
	ds_read_b128 v[4:7], v181 offset:40960
	s_waitcnt vmcnt(6) lgkmcnt(1)
	v_mfma_f32_32x32x16_bf16 v[48:63], v[0:3], v[120:123], v[48:63]
	s_waitcnt lgkmcnt(0)
	v_mfma_f32_32x32x16_bf16 v[64:79], v[4:7], v[120:123], v[64:79]
	ds_read_b128 v[0:3], v182 offset:32768
	ds_read_b128 v[4:7], v182 offset:40960
	s_waitcnt vmcnt(5) lgkmcnt(1)
	v_mfma_f32_32x32x16_bf16 v[48:63], v[0:3], v[116:119], v[48:63]
	s_waitcnt lgkmcnt(0)
	v_mfma_f32_32x32x16_bf16 v[64:79], v[4:7], v[116:119], v[64:79]
	ds_read_b128 v[0:3], v183 offset:32768
	ds_read_b128 v[4:7], v183 offset:40960
	s_waitcnt vmcnt(4) lgkmcnt(1)
	v_mfma_f32_32x32x16_bf16 v[48:63], v[0:3], v[112:115], v[48:63]
	s_waitcnt lgkmcnt(0)
	v_mfma_f32_32x32x16_bf16 v[64:79], v[4:7], v[112:115], v[64:79]
	ds_read_b128 v[0:3], v184 offset:32768
	ds_read_b128 v[4:7], v184 offset:40960
	s_waitcnt vmcnt(3) lgkmcnt(1)
	v_mfma_f32_32x32x16_bf16 v[48:63], v[0:3], v[108:111], v[48:63]
	s_waitcnt lgkmcnt(0)
	v_mfma_f32_32x32x16_bf16 v[64:79], v[4:7], v[108:111], v[64:79]
	ds_read_b128 v[0:3], v185 offset:32768
	ds_read_b128 v[4:7], v185 offset:40960
	s_waitcnt vmcnt(2) lgkmcnt(1)
	v_mfma_f32_32x32x16_bf16 v[48:63], v[0:3], v[104:107], v[48:63]
	s_waitcnt lgkmcnt(0)
	v_mfma_f32_32x32x16_bf16 v[64:79], v[4:7], v[104:107], v[64:79]
	ds_read_b128 v[0:3], v186 offset:32768
	ds_read_b128 v[4:7], v186 offset:40960
	s_waitcnt vmcnt(1) lgkmcnt(1)
	v_mfma_f32_32x32x16_bf16 v[48:63], v[0:3], v[100:103], v[48:63]
	s_waitcnt lgkmcnt(0)
	v_mfma_f32_32x32x16_bf16 v[64:79], v[4:7], v[100:103], v[64:79]
	ds_read_b128 v[0:3], v187 offset:32768
	ds_read_b128 v[4:7], v187 offset:40960
	s_waitcnt vmcnt(0) lgkmcnt(1)
	v_mfma_f32_32x32x16_bf16 v[48:63], v[0:3], v[96:99], v[48:63]
	s_waitcnt lgkmcnt(0)
	v_mfma_f32_32x32x16_bf16 v[64:79], v[4:7], v[96:99], v[64:79]
	ds_read_b128 v[0:3], v191
	ds_read_b128 v[4:7], v190
	ds_read_b128 v[8:11], v191 offset:4096
	ds_read_b128 v[12:15], v190 offset:1024
	s_waitcnt lgkmcnt(2)
	v_mfma_f32_32x32x16_bf16 v[48:63], v[0:3], v[4:7], v[48:63]
	s_waitcnt lgkmcnt(1)
	v_mfma_f32_32x32x16_bf16 v[64:79], v[8:11], v[4:7], v[64:79]
	ds_read_b128 v[0:3], v192
	ds_read_b128 v[4:7], v192 offset:4096
	s_waitcnt lgkmcnt(1)
	v_mfma_f32_32x32x16_bf16 v[48:63], v[0:3], v[12:15], v[48:63]
	s_waitcnt lgkmcnt(0)
	v_mfma_f32_32x32x16_bf16 v[64:79], v[4:7], v[12:15], v[64:79]
	ds_read_b128 v[0:3], v193
	ds_read_b128 v[4:7], v190 offset:2048
	ds_read_b128 v[8:11], v193 offset:4096
	ds_read_b128 v[18:21], v190 offset:3072
	ds_read_b128 v[22:25], v194 offset:4096
	s_waitcnt lgkmcnt(3)
	v_mfma_f32_32x32x16_bf16 v[48:63], v[0:3], v[4:7], v[48:63]
	ds_read_b128 v[0:3], v194
	s_waitcnt lgkmcnt(3)
	v_mfma_f32_32x32x16_bf16 v[64:79], v[8:11], v[4:7], v[64:79]
	s_waitcnt lgkmcnt(0)
	v_mfma_f32_32x32x16_bf16 v[48:63], v[0:3], v[18:21], v[48:63]
	v_mov_b64_e32 v[0:1], s[8:9]
	v_mov_b64_e32 v[2:3], s[10:11]
	v_mov_b64_e32 v[4:5], s[12:13]
	v_mov_b64_e32 v[6:7], s[14:15]
	v_mov_b64_e32 v[8:9], s[16:17]
	v_mov_b64_e32 v[10:11], s[18:19]
	v_mov_b64_e32 v[12:13], s[20:21]
	v_mfma_f32_32x32x16_bf16 v[64:79], v[22:25], v[18:21], v[64:79]
	s_nop 3
	v_max_f32_e32 v18, v49, v49
	v_max_f32_e32 v19, v48, v48
	v_max_f32_e32 v18, v19, v18
	v_max3_f32 v18, v18, v50, v51
	v_max3_f32 v18, v18, v52, v53
	v_max3_f32 v18, v18, v54, v55
	v_max3_f32 v18, v18, v56, v57
	v_max3_f32 v18, v18, v58, v59
	v_max3_f32 v18, v18, v60, v61
	v_max3_f32 v18, v18, v62, v63
	v_max3_f32 v18, v18, v64, v65
	v_max3_f32 v18, v18, v66, v67
	v_max3_f32 v18, v18, v68, v69
	v_max3_f32 v18, v18, v70, v71
	v_max3_f32 v18, v18, v72, v73
	v_max3_f32 v18, v18, v74, v75
	v_max3_f32 v18, v18, v76, v77
	v_max3_f32 v18, v18, v78, v79
	v_mov_b32_e32 v19, v18
	s_nop 1
	v_permlane32_swap_b32_e32 v18, v19
	v_mov_b64_e32 v[14:15], s[22:23]
	s_and_b32 s8, s62, 0x3fffffc0
	v_max_f32_e32 v19, v19, v19
	v_max_f32_e32 v18, v18, v18
	s_lshl_b32 s8, s8, 2
	v_max_f32_e32 v18, v18, v19
	s_add_i32 s12, s8, 0
	v_add_f32_e32 v19, 0x7149f2ca, v18
	s_add_i32 s12, s12, 0x14000
	v_cmp_ge_f32_e32 vcc, s46, v19
	s_cmp_eq_u64 vcc, exec
	s_cselect_b64 vcc, -1, 0
	s_add_i32 s8, s60, 0x4040
	v_max_f32_e32 v128, 0xf149f2ca, v18
	v_lshl_add_u64 v[18:19], s[8:9], 0, v[142:143]
	v_lshl_add_u64 v[20:21], v[146:147], 0, s[8:9]
	v_lshl_add_u64 v[22:23], s[8:9], 0, v[144:145]
	v_lshlrev_b64 v[24:25], 11, v[18:19]
	v_lshlrev_b64 v[26:27], 11, v[20:21]
	v_mad_u64_u32 v[28:29], s[10:11], v18, s44, v[16:17]
	v_mad_u64_u32 v[30:31], s[10:11], v20, s44, v[16:17]
	v_mad_u64_u32 v[16:17], s[10:11], v22, s44, v[16:17]
	v_lshl_add_u64 v[24:25], s[30:31], 0, v[24:25]
	v_lshl_add_u64 v[26:27], s[30:31], 0, v[26:27]
	v_mad_i32_i24 v29, v19, s44, v29
	v_mad_i32_i24 v31, v21, s44, v31
	v_mad_i32_i24 v17, v23, s44, v17
	v_lshl_add_u64 v[18:19], v[24:25], 0, v[150:151]
	v_lshl_add_u64 v[20:21], v[26:27], 0, v[150:151]
	v_lshl_add_u64 v[22:23], v[28:29], 0, v[150:151]
	v_lshl_add_u64 v[24:25], v[30:31], 0, v[150:151]
	v_lshl_add_u64 v[16:17], v[16:17], 0, v[152:153]
	global_load_dwordx4 v[80:83], v[18:19], off
	global_load_dwordx4 v[84:87], v[20:21], off
	global_load_dwordx4 v[88:91], v[22:23], off
	global_load_dwordx4 v[92:95], v[24:25], off
	global_load_dwordx4 v[200:203], v[16:17], off offset:256
	v_sub_f32_e32 v129, 0xf149f2ca, v128
	v_mul_f32_e32 v129, 0x3dd53b94, v129
	v_exp_f32_e32 v164, v129
	v_mov_b32_e32 v129, 0xf149f2ca
	v_cndmask_b32_e32 v198, v128, v129, vcc
	v_mul_f32_e32 v138, 0xbdd53b94, v198
	v_mov_b32_e32 v165, v138
	v_fmamk_f32 v48, v48, 0x3dd53b94, v138
	v_fmamk_f32 v49, v49, 0x3dd53b94, v138
	v_fmamk_f32 v50, v50, 0x3dd53b94, v138
	v_fmamk_f32 v51, v51, 0x3dd53b94, v138
	v_fmamk_f32 v52, v52, 0x3dd53b94, v138
	v_fmamk_f32 v53, v53, 0x3dd53b94, v138
	v_fmamk_f32 v54, v54, 0x3dd53b94, v138
	v_fmamk_f32 v55, v55, 0x3dd53b94, v138
	v_fmamk_f32 v56, v56, 0x3dd53b94, v138
	v_fmamk_f32 v57, v57, 0x3dd53b94, v138
	v_fmamk_f32 v58, v58, 0x3dd53b94, v138
	v_fmamk_f32 v59, v59, 0x3dd53b94, v138
	v_fmamk_f32 v60, v60, 0x3dd53b94, v138
	v_fmamk_f32 v61, v61, 0x3dd53b94, v138
	v_fmamk_f32 v62, v62, 0x3dd53b94, v138
	v_fmac_f32_e32 v165, 0x3dd53b94, v63
	v_exp_f32_e32 v222, v48
	v_exp_f32_e32 v224, v49
	v_exp_f32_e32 v220, v50
	v_exp_f32_e32 v223, v51
	v_exp_f32_e32 v219, v52
	v_exp_f32_e32 v221, v53
	v_exp_f32_e32 v217, v54
	v_exp_f32_e32 v218, v55
	v_exp_f32_e32 v212, v56
	v_exp_f32_e32 v214, v57
	v_exp_f32_e32 v211, v58
	v_exp_f32_e32 v213, v59
	v_exp_f32_e32 v208, v60
	v_exp_f32_e32 v210, v61
	v_exp_f32_e32 v207, v62
	v_exp_f32_e32 v209, v165
	s_waitcnt vmcnt(0)
	v_mov_b64_e32 v[46:47], v[14:15]
	v_mov_b64_e32 v[30:31], v[14:15]
	v_mov_b64_e32 v[62:63], v[14:15]
	s_mov_b32 s8, -1
	v_mov_b64_e32 v[44:45], v[12:13]
	v_mov_b64_e32 v[42:43], v[10:11]
	v_mov_b64_e32 v[40:41], v[8:9]
	v_mov_b64_e32 v[38:39], v[6:7]
	v_mov_b64_e32 v[36:37], v[4:5]
	v_mov_b64_e32 v[34:35], v[2:3]
	v_mov_b64_e32 v[32:33], v[0:1]
	v_mov_b64_e32 v[28:29], v[12:13]
	v_mov_b64_e32 v[26:27], v[10:11]
	v_mov_b64_e32 v[24:25], v[8:9]
	v_mov_b64_e32 v[22:23], v[6:7]
	v_mov_b64_e32 v[20:21], v[4:5]
	v_mov_b64_e32 v[18:19], v[2:3]
	v_mov_b64_e32 v[16:17], v[0:1]
	v_lshl_add_u32 v189, v188, 2, s12
	s_add_i32 s13, s60, 0x4080
	s_add_i32 s83, s60, 0x4040
	s_sub_i32 s14, s61, 64
	v_pk_fma_f32 v[134:135], v[78:79], s[26:27], v[138:139] op_sel_hi:[1,0,0]
	v_pk_fma_f32 v[160:161], v[76:77], s[26:27], v[138:139] op_sel_hi:[1,0,0]
	v_pk_fma_f32 v[162:163], v[74:75], s[26:27], v[138:139] op_sel_hi:[1,0,0]
	v_pk_fma_f32 v[128:129], v[72:73], s[26:27], v[138:139] op_sel_hi:[1,0,0]
	v_pk_fma_f32 v[130:131], v[70:71], s[26:27], v[138:139] op_sel_hi:[1,0,0]
	v_pk_fma_f32 v[132:133], v[68:69], s[26:27], v[138:139] op_sel_hi:[1,0,0]
	v_pk_fma_f32 v[136:137], v[66:67], s[26:27], v[138:139] op_sel_hi:[1,0,0]
	v_pk_fma_f32 v[138:139], v[64:65], s[26:27], v[138:139] op_sel_hi:[1,0,0]
	v_cndmask_b32_e64 v197, v164, 1.0, vcc
	v_mov_b64_e32 v[60:61], v[12:13]
	v_mov_b64_e32 v[58:59], v[10:11]
	v_mov_b64_e32 v[56:57], v[8:9]
	v_mov_b64_e32 v[54:55], v[6:7]
	v_mov_b64_e32 v[52:53], v[4:5]
	v_mov_b64_e32 v[50:51], v[2:3]
	v_mov_b64_e32 v[48:49], v[0:1]
	s_waitcnt vmcnt(4)
	ds_write_b128 v175, v[80:83] offset:16384
	s_waitcnt vmcnt(3)
	ds_write_b128 v176, v[84:87] offset:16384
	s_waitcnt vmcnt(2)
	ds_write_b128 v177, v[88:91] offset:49152
	s_waitcnt vmcnt(1)
	ds_write_b128 v178, v[92:95] offset:49152
	s_waitcnt vmcnt(0)
	ds_write_b128 v196, v[200:203]
	s_nop 0
	s_nop 0
	s_nop 0
	s_nop 0
	s_nop 0
	s_nop 0
	s_nop 0
	s_nop 0
	s_nop 0
	s_nop 0
	s_nop 0
	s_nop 0
	s_waitcnt lgkmcnt(0)
	s_barrier
